# router-constant setup moved from workgroup 0 to the workgroup with one weight strip; conversion loops leave stores in flight
# speedup vs baseline: 1.0066x; 1.0066x over previous
.LBB0_70:
	s_cmp_lg_u32 s96, 0xff
	s_cbranch_scc1 .LBB0_76
	v_and_b32_e32 v8, 31, v0
	v_lshrrev_b32_e32 v9, 5, v0
	v_mov_b32_e32 v3, 0
	v_lshlrev_b32_e32 v2, 9, v9
	v_lshlrev_b32_e32 v10, 2, v8
	v_lshl_add_u64 v[4:5], s[54:55], 0, v[2:3]
	v_lshl_add_u64 v[6:7], s[56:57], 0, v[2:3]
	v_lshl_or_b32 v2, v9, 14, v10
	v_lshl_add_u64 v[8:9], s[58:59], 0, v[2:3]
	s_mov_b64 s[0:1], 0x380
	v_lshl_add_u64 v[8:9], v[8:9], 0, s[0:1]
	s_mov_b64 s[0:1], 0
	s_mov_b64 s[4:5], 0x400
	v_mov_b32_e32 v2, v3

.LBB0_185:
	v_readlane_b32 s0, v254, 11
	v_mov_b32_e32 v54, v0
	s_mov_b32 s2, s0
	s_cmpk_gt_i32 s0, 0x1fff
	v_readlane_b32 s1, v254, 12
	s_cbranch_scc1 .LBB0_195
	s_add_u32 s5, s92, 0x9400000
	s_addc_u32 s6, s93, 0
	s_lshr_b32 s0, s51, 19
	s_add_i32 s0, s2, s0
	s_and_b32 s0, s0, 0xffffe000
	s_sub_i32 s1, s2, s0
	s_sext_i32_i16 s0, s1
	s_bfe_u32 s0, s0, 0x80017
	s_add_i32 s0, s1, s0
	s_sext_i32_i16 s4, s0
	s_lshr_b32 s0, s4, 8
	s_and_b32 s4, s4, 0xffffff00
	s_sub_i32 s4, s1, s4
	s_bfe_u32 s1, s4, 0x4001b
	s_add_i32 s1, s4, s1
	s_sext_i32_i16 s1, s1
	s_ashr_i32 s8, s1, 4
	s_bfe_i64 s[0:1], s[0:1], 0x100000
	s_lshl_b64 s[0:1], s[0:1], 25
	s_add_u32 s9, s62, s0
	s_addc_u32 s10, s63, s1
	s_lshl_b32 s0, s8, 7
	s_lshl_b32 s7, s86, 4
	s_add_i32 s0, s7, s0
	s_ashr_i32 s1, s0, 31
	s_lshl_b64 s[0:1], s[0:1], 14
	s_add_u32 s9, s9, s0
	s_addc_u32 s10, s10, s1
	s_lshl_b32 s0, s8, 12
	s_lshl_b32 s1, s4, 8
	s_sub_i32 s0, s1, s0
	s_ashr_i32 s1, s0, 31
	s_lshl_b64 s[0:1], s[0:1], 2
	v_and_b32_e32 v55, 63, v54
	s_add_u32 s0, s9, s0
	s_addc_u32 s1, s10, s1
	v_lshlrev_b32_e32 v130, 4, v55
	v_mov_b32_e32 v131, 0
	v_lshl_add_u64 v[30:31], s[0:1], 0, v[130:131]
	s_movk_i32 s8, 0x4000
	v_add_co_u32_e32 v2, vcc, s8, v30
	s_mov_b32 s9, 0x8000
	s_nop 0
	v_addc_co_u32_e32 v3, vcc, 0, v31, vcc
	v_add_co_u32_e32 v6, vcc, s9, v30
	s_mov_b32 s10, 0xc000
	s_nop 0
	v_addc_co_u32_e32 v7, vcc, 0, v31, vcc
	v_add_co_u32_e32 v10, vcc, s10, v30
	s_mov_b32 s11, 0x10000
	s_nop 0
	v_addc_co_u32_e32 v11, vcc, 0, v31, vcc
	v_add_co_u32_e32 v14, vcc, s11, v30
	s_mov_b32 s12, 0x14000
	s_nop 0
	v_addc_co_u32_e32 v15, vcc, 0, v31, vcc
	v_add_co_u32_e32 v18, vcc, s12, v30
	s_mov_b32 s13, 0x18000
	s_nop 0
	v_addc_co_u32_e32 v19, vcc, 0, v31, vcc
	v_add_co_u32_e32 v22, vcc, s13, v30
	s_mov_b32 s14, 0x1c000
	s_nop 0
	v_addc_co_u32_e32 v23, vcc, 0, v31, vcc
	v_add_co_u32_e32 v26, vcc, s14, v30
	s_mov_b32 s15, 0x20000
	s_nop 0
	v_addc_co_u32_e32 v27, vcc, 0, v31, vcc
	v_add_co_u32_e32 v32, vcc, s15, v30
	s_mov_b32 s20, 0x24000
	s_nop 0
	v_addc_co_u32_e32 v33, vcc, 0, v31, vcc
	global_load_dwordx4 v[2:5], v[2:3], off nt
	s_nop 0
	global_load_dwordx4 v[6:9], v[6:7], off nt
	s_nop 0
	global_load_dwordx4 v[10:13], v[10:11], off nt
	s_nop 0
	global_load_dwordx4 v[14:17], v[14:15], off nt
	s_nop 0
	global_load_dwordx4 v[18:21], v[18:19], off nt
	s_nop 0
	global_load_dwordx4 v[22:25], v[22:23], off nt
	s_nop 0
	global_load_dwordx4 v[26:29], v[26:27], off nt
	s_nop 0
	global_load_dwordx4 v[34:37], v[32:33], off nt
	v_add_co_u32_e32 v32, vcc, s20, v30
	s_mov_b32 s21, 0x28000
	s_nop 0
	v_addc_co_u32_e32 v33, vcc, 0, v31, vcc
	v_add_co_u32_e32 v42, vcc, s21, v30
	s_mov_b32 s22, 0x2c000
	s_nop 0
	v_addc_co_u32_e32 v43, vcc, 0, v31, vcc
	global_load_dwordx4 v[38:41], v[32:33], off nt
	s_nop 0
	global_load_dwordx4 v[42:45], v[42:43], off nt
	v_add_co_u32_e32 v32, vcc, s22, v30
	s_mov_b32 s23, 0x30000
	s_nop 0
	v_addc_co_u32_e32 v33, vcc, 0, v31, vcc
	v_add_co_u32_e32 v50, vcc, s23, v30
	s_mov_b32 s4, 0x34000
	s_nop 0
	v_addc_co_u32_e32 v51, vcc, 0, v31, vcc
	global_load_dwordx4 v[46:49], v[32:33], off nt
	s_nop 0
	global_load_dwordx4 v[50:53], v[50:51], off nt
	v_add_co_u32_e32 v32, vcc, s4, v30
	s_mov_b32 s4, 0x38000
	s_nop 0
	v_addc_co_u32_e32 v33, vcc, 0, v31, vcc
	v_add_co_u32_e32 v56, vcc, s4, v30
	s_mov_b32 s4, 0x3c000
	s_nop 0
	v_addc_co_u32_e32 v57, vcc, 0, v31, vcc
	global_load_dwordx4 v[62:65], v[32:33], off nt
	global_load_dwordx4 v[74:77], v[56:57], off nt
	v_add_co_u32_e32 v56, vcc, s4, v30
	v_lshrrev_b32_e32 v58, 7, v54
	s_nop 0
	v_addc_co_u32_e32 v57, vcc, 0, v31, vcc
	global_load_dwordx4 v[30:33], v130, s[0:1] nt
	global_load_dwordx4 v[86:89], v[56:57], off nt
	v_xor_b32_e32 v58, v58, v54
	v_lshlrev_b32_e32 v58, 4, v58
	v_and_b32_e32 v132, 0x70, v58
	v_add_u32_e32 v58, 0x200, v54
	v_ashrrev_i32_e32 v140, 3, v58
	v_lshrrev_b32_e32 v58, 7, v58
	v_xor_b32_e32 v58, v58, v54
	v_lshlrev_b32_e32 v58, 4, v58
	v_add_u32_e32 v61, 0x600, v54
	s_movk_i32 s0, 0x240
	v_lshrrev_b32_e32 v56, 2, v54
	v_lshlrev_b32_e32 v57, 4, v54
	v_and_b32_e32 v134, 0x70, v58
	v_add_u32_e32 v58, 0x400, v54
	v_ashrrev_i32_e32 v144, 3, v61
	v_lshrrev_b32_e32 v61, 7, v61
	v_mad_u32_u24 v55, v55, s0, 0
	v_bitop3_b32 v56, v56, s86, 7 bitop3:0x6c
	v_and_b32_e32 v57, 0x70, v57
	v_ashrrev_i32_e32 v138, 3, v54
	s_movk_i32 s0, 0x90
	v_ashrrev_i32_e32 v142, 3, v58
	v_xor_b32_e32 v54, v61, v54
	v_lshlrev_b32_e32 v56, 4, v56
	v_add_u32_e32 v57, 0, v57
	v_mul_lo_u32 v59, v138, s0
	v_mul_lo_u32 v60, v140, s0
	v_mul_lo_u32 v58, v142, s0
	v_mul_lo_u32 v61, v144, s0
	v_lshlrev_b32_e32 v54, 4, v54
	v_and_b32_e32 v139, 0x7f, v138
	v_mov_b32_e32 v133, v131
	v_and_b32_e32 v141, 0x7f, v140
	v_mov_b32_e32 v135, v131
	v_and_b32_e32 v143, 0x7f, v142
	v_and_b32_e32 v145, 0x7f, v144
	v_and_b32_e32 v136, 0x70, v54
	v_mov_b32_e32 v137, v131
	s_lshl_b32 s24, s90, 1
	v_add_u32_e32 v146, v55, v56
	v_add_u32_e32 v147, v57, v59
	v_add_u32_e32 v148, v57, v60
	v_add_u32_e32 v149, v57, v58
	v_add_u32_e32 v150, v57, v61
	s_mov_b32 s25, s2
	s_waitcnt vmcnt(0)
	s_branch .LBB0_189

.LBB0_189:
	s_add_i32 s26, s25, s90
	s_cmpk_lt_i32 s26, 0x2000
	s_cselect_b64 s[0:1], -1, 0
	s_cmpk_gt_i32 s26, 0x1fff
	s_cbranch_scc1 .LBB0_191
	s_ashr_i32 s4, s26, 31
	s_lshr_b32 s4, s4, 19
	s_add_i32 s4, s26, s4
	s_and_b32 s4, s4, 0xffffe000
	s_sub_i32 s27, s26, s4
	s_sext_i32_i16 s4, s27
	s_bfe_u32 s4, s4, 0x80017
	s_add_i32 s4, s27, s4
	s_sext_i32_i16 s28, s4
	s_lshr_b32 s4, s28, 8
	s_and_b32 s28, s28, 0xffffff00
	s_sub_i32 s27, s27, s28
	s_bfe_u32 s28, s27, 0x4001b
	s_add_i32 s28, s27, s28
	s_sext_i32_i16 s28, s28
	s_ashr_i32 s30, s28, 4
	s_bfe_i64 s[28:29], s[4:5], 0x100000
	s_lshl_b64 s[28:29], s[28:29], 25
	s_add_u32 s4, s62, s28
	s_addc_u32 s31, s63, s29
	s_lshl_b32 s28, s30, 7
	s_add_i32 s28, s28, s7
	s_ashr_i32 s29, s28, 31
	s_lshl_b64 s[28:29], s[28:29], 14
	s_add_u32 s4, s4, s28
	s_addc_u32 s31, s31, s29
	s_lshl_b32 s28, s30, 12
	s_lshl_b32 s27, s27, 8
	s_sub_i32 s28, s27, s28
	s_ashr_i32 s29, s28, 31
	s_lshl_b64 s[28:29], s[28:29], 2
	s_add_u32 s28, s4, s28
	s_addc_u32 s29, s31, s29
	v_lshl_add_u64 v[122:123], s[28:29], 0, v[130:131]
	v_add_co_u32_e32 v58, vcc, s8, v122
	s_nop 1
	v_addc_co_u32_e32 v59, vcc, 0, v123, vcc
	v_add_co_u32_e32 v66, vcc, s9, v122
	global_load_dwordx4 v[54:57], v[122:123], off nt
	s_nop 0
	global_load_dwordx4 v[58:61], v[58:59], off nt
	v_addc_co_u32_e32 v67, vcc, 0, v123, vcc
	v_add_co_u32_e32 v70, vcc, s10, v122
	s_nop 1
	v_addc_co_u32_e32 v71, vcc, 0, v123, vcc
	v_add_co_u32_e32 v78, vcc, s11, v122
	global_load_dwordx4 v[66:69], v[66:67], off nt
	s_nop 0
	global_load_dwordx4 v[70:73], v[70:71], off nt
	v_addc_co_u32_e32 v79, vcc, 0, v123, vcc
	v_add_co_u32_e32 v82, vcc, s12, v122
	s_nop 1
	v_addc_co_u32_e32 v83, vcc, 0, v123, vcc
	v_add_co_u32_e32 v90, vcc, s13, v122
	global_load_dwordx4 v[78:81], v[78:79], off nt
	s_nop 0
	global_load_dwordx4 v[82:85], v[82:83], off nt
	v_addc_co_u32_e32 v91, vcc, 0, v123, vcc
	v_add_co_u32_e32 v94, vcc, s14, v122
	s_nop 1
	v_addc_co_u32_e32 v95, vcc, 0, v123, vcc
	v_add_co_u32_e32 v98, vcc, s15, v122
	global_load_dwordx4 v[90:93], v[90:91], off nt
	s_nop 0
	global_load_dwordx4 v[94:97], v[94:95], off nt
	v_addc_co_u32_e32 v99, vcc, 0, v123, vcc
	v_add_co_u32_e32 v102, vcc, s20, v122
	s_nop 1
	v_addc_co_u32_e32 v103, vcc, 0, v123, vcc
	s_waitcnt lgkmcnt(0)
	v_add_co_u32_e32 v106, vcc, s21, v122
	global_load_dwordx4 v[98:101], v[98:99], off nt
	s_nop 0
	global_load_dwordx4 v[102:105], v[102:103], off nt
	v_addc_co_u32_e32 v107, vcc, 0, v123, vcc
	v_add_co_u32_e32 v110, vcc, s22, v122
	s_nop 1
	v_addc_co_u32_e32 v111, vcc, 0, v123, vcc
	v_add_co_u32_e32 v114, vcc, 0x30000, v122
	global_load_dwordx4 v[106:109], v[106:107], off nt
	s_nop 0
	global_load_dwordx4 v[110:113], v[110:111], off nt
	v_addc_co_u32_e32 v115, vcc, 0, v123, vcc
	v_add_co_u32_e32 v118, vcc, 0x34000, v122
	s_nop 1
	v_addc_co_u32_e32 v119, vcc, 0, v123, vcc
	v_add_co_u32_e32 v124, vcc, 0x38000, v122
	global_load_dwordx4 v[114:117], v[114:115], off nt
	s_nop 0
	global_load_dwordx4 v[118:121], v[118:119], off nt
	v_addc_co_u32_e32 v125, vcc, 0, v123, vcc
	v_add_co_u32_e32 v126, vcc, 0x3c000, v122
	s_nop 1
	v_addc_co_u32_e32 v127, vcc, 0, v123, vcc
	global_load_dwordx4 v[122:125], v[124:125], off nt
	s_nop 0
	global_load_dwordx4 v[126:129], v[126:127], off nt
	s_waitcnt vmcnt(20)
	s_branch .Lcvgu_a

.LBB0_930:
	v_readlane_b32 s0, v254, 11
	v_mov_b32_e32 v50, v0
	s_cmpk_gt_i32 s0, 0xfff
	v_readlane_b32 s1, v254, 12
	s_cbranch_scc1 .LBB0_939
	s_add_u32 s5, s92, 0x29400000
	v_readlane_b32 s0, v254, 11
	s_addc_u32 s6, s93, 0
	s_mov_b32 s2, s0
	s_ashr_i32 s0, s0, 31
	s_lshr_b32 s0, s0, 20
	s_add_i32 s0, s2, s0
	v_readlane_b32 s1, v254, 12
	s_and_b32 s0, s0, 0xfffff000
	s_sub_i32 s1, s2, s0
	s_sext_i32_i16 s0, s1
	s_bfe_u32 s0, s0, 0x70018
	s_add_i32 s0, s1, s0
	s_sext_i32_i16 s4, s0
	s_lshr_b32 s0, s4, 7
	s_and_b32 s4, s4, 0xffffff80
	s_sub_i32 s4, s1, s4
	s_bfe_u32 s1, s4, 0x3001c
	s_add_i32 s1, s4, s1
	s_sext_i32_i16 s1, s1
	s_ashr_i32 s8, s1, 3
	s_bfe_i64 s[0:1], s[0:1], 0x100000
	v_readlane_b32 s36, v254, 32
	s_lshl_b64 s[0:1], s[0:1], 24
	v_readlane_b32 s50, v254, 46
	v_readlane_b32 s51, v254, 47
	s_add_u32 s9, s50, s0
	s_addc_u32 s10, s51, s1
	s_lshl_b32 s0, s8, 7
	s_lshl_b32 s7, s86, 4
	s_add_i32 s0, s7, s0
	s_ashr_i32 s1, s0, 31
	s_lshl_b64 s[0:1], s[0:1], 13
	s_add_u32 s9, s9, s0
	s_addc_u32 s10, s10, s1
	s_lshl_b32 s0, s8, 11
	s_lshl_b32 s1, s4, 8
	s_sub_i32 s0, s1, s0
	s_ashr_i32 s1, s0, 31
	s_lshl_b64 s[0:1], s[0:1], 2
	v_and_b32_e32 v51, 63, v50
	s_add_u32 s0, s9, s0
	s_addc_u32 s1, s10, s1
	v_lshlrev_b32_e32 v130, 4, v51
	v_mov_b32_e32 v131, 0
	v_lshl_add_u64 v[30:31], s[0:1], 0, v[130:131]
	s_movk_i32 s8, 0x2000
	v_add_co_u32_e32 v10, vcc, s8, v30
	s_movk_i32 s9, 0x4000
	s_nop 0
	v_addc_co_u32_e32 v11, vcc, 0, v31, vcc
	v_add_co_u32_e32 v12, vcc, s9, v30
	s_movk_i32 s10, 0x6000
	s_nop 0
	v_addc_co_u32_e32 v13, vcc, 0, v31, vcc
	global_load_dwordx4 v[2:5], v[10:11], off nt
	global_load_dwordx4 v[6:9], v[12:13], off nt
	v_add_co_u32_e32 v10, vcc, s10, v30
	s_mov_b32 s11, 0x8000
	s_nop 0
	v_addc_co_u32_e32 v11, vcc, 0, v31, vcc
	v_add_co_u32_e32 v14, vcc, s11, v30
	s_mov_b32 s16, 0xa000
	s_nop 0
	v_addc_co_u32_e32 v15, vcc, 0, v31, vcc
	v_add_co_u32_e32 v18, vcc, s16, v30
	s_mov_b32 s17, 0xc000
	s_nop 0
	v_addc_co_u32_e32 v19, vcc, 0, v31, vcc
	v_add_co_u32_e32 v22, vcc, s17, v30
	s_mov_b32 s18, 0xe000
	s_nop 0
	v_addc_co_u32_e32 v23, vcc, 0, v31, vcc
	v_add_co_u32_e32 v26, vcc, s18, v30
	s_mov_b32 s19, 0x10000
	s_nop 0
	v_addc_co_u32_e32 v27, vcc, 0, v31, vcc
	v_add_co_u32_e32 v32, vcc, s19, v30
	s_mov_b32 s20, 0x12000
	s_nop 0
	v_addc_co_u32_e32 v33, vcc, 0, v31, vcc
	global_load_dwordx4 v[10:13], v[10:11], off nt
	s_nop 0
	global_load_dwordx4 v[14:17], v[14:15], off nt
	s_nop 0
	global_load_dwordx4 v[18:21], v[18:19], off nt
	s_nop 0
	global_load_dwordx4 v[22:25], v[22:23], off nt
	s_nop 0
	global_load_dwordx4 v[26:29], v[26:27], off nt
	s_nop 0
	global_load_dwordx4 v[34:37], v[32:33], off nt
	v_add_co_u32_e32 v32, vcc, s20, v30
	s_mov_b32 s22, 0x14000
	s_nop 0
	v_addc_co_u32_e32 v33, vcc, 0, v31, vcc
	v_add_co_u32_e32 v42, vcc, s22, v30
	s_mov_b32 s24, 0x16000
	s_nop 0
	v_addc_co_u32_e32 v43, vcc, 0, v31, vcc
	global_load_dwordx4 v[38:41], v[32:33], off nt
	s_nop 0
	global_load_dwordx4 v[42:45], v[42:43], off nt
	v_add_co_u32_e32 v32, vcc, s24, v30
	s_mov_b32 s25, 0x18000
	s_nop 0
	v_addc_co_u32_e32 v33, vcc, 0, v31, vcc
	v_add_co_u32_e32 v52, vcc, s25, v30
	s_mov_b32 s4, 0x1a000
	s_nop 0
	v_addc_co_u32_e32 v53, vcc, 0, v31, vcc
	global_load_dwordx4 v[46:49], v[32:33], off nt
	global_load_dwordx4 v[54:57], v[52:53], off nt
	v_add_co_u32_e32 v32, vcc, s4, v30
	s_mov_b32 s4, 0x1c000
	s_nop 0
	v_addc_co_u32_e32 v33, vcc, 0, v31, vcc
	v_add_co_u32_e32 v52, vcc, s4, v30
	s_mov_b32 s4, 0x1e000
	s_nop 0
	v_addc_co_u32_e32 v53, vcc, 0, v31, vcc
	global_load_dwordx4 v[66:69], v[32:33], off nt
	global_load_dwordx4 v[78:81], v[52:53], off nt
	v_add_co_u32_e32 v52, vcc, s4, v30
	v_lshrrev_b32_e32 v58, 7, v50
	s_nop 0
	v_addc_co_u32_e32 v53, vcc, 0, v31, vcc
	global_load_dwordx4 v[30:33], v130, s[0:1] nt
	global_load_dwordx4 v[90:93], v[52:53], off nt
	v_xor_b32_e32 v58, v58, v50
	v_lshlrev_b32_e32 v58, 4, v58
	v_and_b32_e32 v132, 0x70, v58
	v_add_u32_e32 v58, 0x200, v50
	v_ashrrev_i32_e32 v139, 3, v58
	v_lshrrev_b32_e32 v58, 7, v58
	v_xor_b32_e32 v58, v58, v50
	v_lshlrev_b32_e32 v58, 4, v58
	v_add_u32_e32 v61, 0x600, v50
	s_movk_i32 s0, 0x240
	v_lshrrev_b32_e32 v52, 2, v50
	v_lshlrev_b32_e32 v53, 4, v50
	v_and_b32_e32 v134, 0x70, v58
	v_add_u32_e32 v58, 0x400, v50
	v_ashrrev_i32_e32 v141, 3, v61
	v_lshrrev_b32_e32 v61, 7, v61
	v_mad_u32_u24 v51, v51, s0, 0
	v_bitop3_b32 v52, v52, s86, 7 bitop3:0x6c
	v_and_b32_e32 v53, 0x70, v53
	v_ashrrev_i32_e32 v138, 3, v50
	s_movk_i32 s0, 0x90
	v_ashrrev_i32_e32 v140, 3, v58
	v_xor_b32_e32 v50, v61, v50
	v_lshlrev_b32_e32 v52, 4, v52
	v_add_u32_e32 v53, 0, v53
	v_mul_lo_u32 v59, v138, s0
	v_mul_lo_u32 v60, v139, s0
	v_mul_lo_u32 v58, v140, s0
	v_mul_lo_u32 v61, v141, s0
	v_lshlrev_b32_e32 v50, 4, v50
	v_mov_b32_e32 v133, v131
	v_mov_b32_e32 v135, v131
	v_and_b32_e32 v136, 0x70, v50
	v_mov_b32_e32 v137, v131
	s_lshl_b32 s26, s90, 1
	v_add_u32_e32 v142, v51, v52
	v_add_u32_e32 v143, v53, v59
	v_add_u32_e32 v144, v53, v60
	v_add_u32_e32 v145, v53, v58
	v_add_u32_e32 v146, v53, v61
	s_mov_b32 s27, s2
	v_readlane_b32 s37, v254, 33
	v_readlane_b32 s38, v254, 34
	v_readlane_b32 s39, v254, 35
	v_readlane_b32 s40, v254, 36
	v_readlane_b32 s41, v254, 37
	v_readlane_b32 s42, v254, 38
	v_readlane_b32 s43, v254, 39
	v_readlane_b32 s44, v254, 40
	v_readlane_b32 s45, v254, 41
	v_readlane_b32 s46, v254, 42
	v_readlane_b32 s47, v254, 43
	v_readlane_b32 s48, v254, 44
	v_readlane_b32 s49, v254, 45
	s_waitcnt vmcnt(0)
	s_branch .LBB0_934

.LBB0_934:
	s_add_i32 s28, s27, s90
	s_cmpk_lt_i32 s28, 0x1000
	s_cselect_b64 s[0:1], -1, 0
	s_cmpk_gt_i32 s28, 0xfff
	s_cbranch_scc1 .LBB0_936
	s_ashr_i32 s4, s28, 31
	s_lshr_b32 s4, s4, 20
	s_add_i32 s4, s28, s4
	s_and_b32 s4, s4, 0xfffff000
	s_sub_i32 s29, s28, s4
	s_sext_i32_i16 s4, s29
	s_bfe_u32 s4, s4, 0x70018
	s_add_i32 s4, s29, s4
	s_sext_i32_i16 s30, s4
	s_lshr_b32 s4, s30, 7
	s_and_b32 s30, s30, 0xffffff80
	s_sub_i32 s29, s29, s30
	s_bfe_u32 s30, s29, 0x3001c
	s_add_i32 s30, s29, s30
	s_sext_i32_i16 s30, s30
	s_ashr_i32 s34, s30, 3
	s_bfe_i64 s[30:31], s[4:5], 0x100000
	v_readlane_b32 s36, v254, 32
	s_lshl_b64 s[30:31], s[30:31], 24
	v_readlane_b32 s50, v254, 46
	v_readlane_b32 s51, v254, 47
	s_add_u32 s4, s50, s30
	s_addc_u32 s35, s51, s31
	s_lshl_b32 s30, s34, 7
	s_add_i32 s30, s30, s7
	s_ashr_i32 s31, s30, 31
	s_lshl_b64 s[30:31], s[30:31], 13
	s_add_u32 s4, s4, s30
	s_addc_u32 s35, s35, s31
	s_lshl_b32 s30, s34, 11
	s_lshl_b32 s29, s29, 8
	s_sub_i32 s30, s29, s30
	s_ashr_i32 s31, s30, 31
	s_lshl_b64 s[30:31], s[30:31], 2
	s_add_u32 s30, s4, s30
	s_addc_u32 s31, s35, s31
	v_lshl_add_u64 v[122:123], s[30:31], 0, v[130:131]
	v_add_co_u32_e32 v58, vcc, s8, v122
	v_readlane_b32 s37, v254, 33
	s_nop 0
	v_addc_co_u32_e32 v59, vcc, 0, v123, vcc
	v_add_co_u32_e32 v62, vcc, s9, v122
	global_load_dwordx4 v[50:53], v[122:123], off nt
	s_nop 0
	global_load_dwordx4 v[58:61], v[58:59], off nt
	v_addc_co_u32_e32 v63, vcc, 0, v123, vcc
	v_add_co_u32_e32 v70, vcc, s10, v122
	v_readlane_b32 s38, v254, 34
	s_nop 0
	v_addc_co_u32_e32 v71, vcc, 0, v123, vcc
	v_add_co_u32_e32 v74, vcc, s11, v122
	global_load_dwordx4 v[62:65], v[62:63], off nt
	s_nop 0
	global_load_dwordx4 v[70:73], v[70:71], off nt
	v_addc_co_u32_e32 v75, vcc, 0, v123, vcc
	v_add_co_u32_e32 v82, vcc, s16, v122
	v_readlane_b32 s39, v254, 35
	s_nop 0
	v_addc_co_u32_e32 v83, vcc, 0, v123, vcc
	v_add_co_u32_e32 v86, vcc, s17, v122
	global_load_dwordx4 v[74:77], v[74:75], off nt
	s_nop 0
	global_load_dwordx4 v[82:85], v[82:83], off nt
	v_addc_co_u32_e32 v87, vcc, 0, v123, vcc
	v_add_co_u32_e32 v94, vcc, s18, v122
	v_readlane_b32 s40, v254, 36
	s_nop 0
	v_addc_co_u32_e32 v95, vcc, 0, v123, vcc
	v_add_co_u32_e32 v98, vcc, s19, v122
	global_load_dwordx4 v[86:89], v[86:87], off nt
	s_nop 0
	global_load_dwordx4 v[94:97], v[94:95], off nt
	v_addc_co_u32_e32 v99, vcc, 0, v123, vcc
	v_add_co_u32_e32 v102, vcc, s20, v122
	v_readlane_b32 s41, v254, 37
	s_nop 0
	v_addc_co_u32_e32 v103, vcc, 0, v123, vcc
	v_add_co_u32_e32 v106, vcc, s22, v122
	global_load_dwordx4 v[98:101], v[98:99], off nt
	s_nop 0
	global_load_dwordx4 v[102:105], v[102:103], off nt
	v_addc_co_u32_e32 v107, vcc, 0, v123, vcc
	v_add_co_u32_e32 v110, vcc, s24, v122
	v_readlane_b32 s42, v254, 38
	s_nop 0
	v_addc_co_u32_e32 v111, vcc, 0, v123, vcc
	v_add_co_u32_e32 v114, vcc, 0x18000, v122
	global_load_dwordx4 v[106:109], v[106:107], off nt
	s_nop 0
	global_load_dwordx4 v[110:113], v[110:111], off nt
	v_addc_co_u32_e32 v115, vcc, 0, v123, vcc
	v_add_co_u32_e32 v118, vcc, 0x1a000, v122
	v_readlane_b32 s43, v254, 39
	s_nop 0
	v_addc_co_u32_e32 v119, vcc, 0, v123, vcc
	v_add_co_u32_e32 v124, vcc, 0x1c000, v122
	global_load_dwordx4 v[114:117], v[114:115], off nt
	s_nop 0
	global_load_dwordx4 v[118:121], v[118:119], off nt
	v_addc_co_u32_e32 v125, vcc, 0, v123, vcc
	v_add_co_u32_e32 v126, vcc, 0x1e000, v122
	v_readlane_b32 s44, v254, 40
	s_nop 0
	v_addc_co_u32_e32 v127, vcc, 0, v123, vcc
	global_load_dwordx4 v[122:125], v[124:125], off nt
	s_nop 0
	global_load_dwordx4 v[126:129], v[126:127], off nt
	v_readlane_b32 s45, v254, 41
	v_readlane_b32 s46, v254, 42
	v_readlane_b32 s47, v254, 43
	v_readlane_b32 s48, v254, 44
	v_readlane_b32 s49, v254, 45
	s_waitcnt vmcnt(20)
	s_branch .Lcvdn_a
